# wconv: src/dst pointers for both layers fetched in one scalar-load batch with mbase, selected by s_cselect (one kernarg round trip instead of two dependent ones); LN DPP reduction kept
# baseline (speedup 1.0000x reference)
_Z12wconv_kernel5WDesci:
	s_movk_i32 s5, 0x800
	s_cmp_lt_u32 s3, 5
	s_cselect_b32 s4, 0x200, s5
	s_cmp_ge_u32 s2, s4
	s_cbranch_scc1 .Lwc_exit
	s_mov_b32 s4, s2
	s_load_dword s8, s[0:1], 0x150
	s_lshl_b32 s14, s3, 3
	s_add_u32 s14, s0, s14
	s_addc_u32 s15, s1, 0
	s_load_dwordx2 s[16:17], s[14:15], 0x0
	s_load_dwordx2 s[18:19], s[14:15], 0x70
	s_load_dwordx2 s[30:31], s[14:15], 0x38
	s_load_dwordx2 s[32:33], s[14:15], 0xa8
	s_cmp_eq_u32 s3, 5
	s_cselect_b32 s9, 13, 11
	s_cmp_eq_u32 s3, 6
	s_cselect_b32 s10, 13, 11
	s_sub_u32 s11, s9, 7
	s_lshr_b32 s12, s4, s11
	s_lshl_b32 s13, s12, s11
	s_sub_u32 s13, s4, s13
	s_add_u32 s20, s9, 2
	s_add_u32 s21, s10, 1
	v_lshrrev_b32_e32 v4, 5, v0
	v_and_b32_e32 v6, 31, v0
	v_lshlrev_b32_e32 v5, 3, v4
	v_lshlrev_b32_e32 v5, s20, v5
	v_lshl_add_u32 v1, v6, 4, v5
	v_and_b32_e32 v8, 7, v6
	v_xor_b32_e32 v7, v4, v8
	v_lshlrev_b32_e32 v7, 4, v7
	v_lshl_add_u32 v2, v6, 9, v7
	v_lshrrev_b32_e32 v9, 3, v0
	v_and_b32_e32 v10, 7, v0
	v_xor_b32_e32 v11, v10, v4
	v_lshlrev_b32_e32 v11, 4, v11
	v_lshl_add_u32 v52, v9, 7, v11
	v_lshlrev_b32_e32 v12, s21, v9
	v_lshl_add_u32 v53, v10, 4, v12
	s_add_u32 s22, s20, 6
	s_lshl_b32 s23, s12, s22
	s_lshl_b32 s24, s13, 9
	s_add_u32 s23, s23, s24
	s_lshl_b32 s25, 1, s20
	s_add_u32 s26, s21, 7
	s_lshl_b32 s27, s13, s26
	s_lshl_b32 s28, s12, 7
	s_add_u32 s27, s27, s28
	s_add_u32 s29, s10, 6
	s_lshl_b32 s29, 1, s29
	s_waitcnt lgkmcnt(0)
	s_cmp_eq_u32 s8, 0
	s_cselect_b32 s16, s16, s30
	s_cselect_b32 s17, s17, s31
	s_cselect_b32 s18, s18, s32
	s_cselect_b32 s19, s19, s33
	s_add_u32 s16, s16, s23
	s_addc_u32 s17, s17, 0
	s_add_u32 s18, s18, s27
	s_addc_u32 s19, s19, 0
	global_load_dwordx4 v[4:7], v1, s[16:17] sc1 nt
	s_add_u32 s16, s16, s25
	s_addc_u32 s17, s17, 0
	global_load_dwordx4 v[8:11], v1, s[16:17] sc1 nt
	s_add_u32 s16, s16, s25
	s_addc_u32 s17, s17, 0
	global_load_dwordx4 v[12:15], v1, s[16:17] sc1 nt
	s_add_u32 s16, s16, s25
	s_addc_u32 s17, s17, 0
	global_load_dwordx4 v[16:19], v1, s[16:17] sc1 nt
	s_add_u32 s16, s16, s25
	s_addc_u32 s17, s17, 0
	global_load_dwordx4 v[20:23], v1, s[16:17] sc1 nt
	s_add_u32 s16, s16, s25
	s_addc_u32 s17, s17, 0
	global_load_dwordx4 v[24:27], v1, s[16:17] sc1 nt
	s_add_u32 s16, s16, s25
	s_addc_u32 s17, s17, 0
	global_load_dwordx4 v[28:31], v1, s[16:17] sc1 nt
	s_add_u32 s16, s16, s25
	s_addc_u32 s17, s17, 0
	global_load_dwordx4 v[32:35], v1, s[16:17] sc1 nt
	s_waitcnt vmcnt(6)
	v_cvt_pk_f16_f32 v36, v4, v8
	v_cvt_pk_f16_f32 v40, v5, v9
	v_cvt_pk_f16_f32 v44, v6, v10
	v_cvt_pk_f16_f32 v48, v7, v11
	s_waitcnt vmcnt(4)
	v_cvt_pk_f16_f32 v37, v12, v16
	v_cvt_pk_f16_f32 v41, v13, v17
	v_cvt_pk_f16_f32 v45, v14, v18
	v_cvt_pk_f16_f32 v49, v15, v19
	s_waitcnt vmcnt(2)
	v_cvt_pk_f16_f32 v38, v20, v24
	v_cvt_pk_f16_f32 v42, v21, v25
	v_cvt_pk_f16_f32 v46, v22, v26
	v_cvt_pk_f16_f32 v50, v23, v27
	s_waitcnt vmcnt(0)
	v_cvt_pk_f16_f32 v39, v28, v32
	v_cvt_pk_f16_f32 v43, v29, v33
	v_cvt_pk_f16_f32 v47, v30, v34
	v_cvt_pk_f16_f32 v51, v31, v35
	ds_write_b128 v2, v[36:39]
	ds_write_b128 v2, v[40:43] offset:128
	ds_write_b128 v2, v[44:47] offset:256
	ds_write_b128 v2, v[48:51] offset:384
	s_waitcnt lgkmcnt(0)
	s_barrier
	ds_read_b128 v[4:7], v52
	ds_read_b128 v[8:11], v52 offset:4096
	ds_read_b128 v[12:15], v52 offset:8192
	ds_read_b128 v[16:19], v52 offset:12288
	s_waitcnt lgkmcnt(3)
	global_store_dwordx4 v53, v[4:7], s[18:19] sc1
	s_add_u32 s18, s18, s29
	s_addc_u32 s19, s19, 0
	s_waitcnt lgkmcnt(2)
	global_store_dwordx4 v53, v[8:11], s[18:19] sc1
	s_add_u32 s18, s18, s29
	s_addc_u32 s19, s19, 0
	s_waitcnt lgkmcnt(1)
	global_store_dwordx4 v53, v[12:15], s[18:19] sc1
	s_add_u32 s18, s18, s29
	s_addc_u32 s19, s19, 0
	s_waitcnt lgkmcnt(0)
	global_store_dwordx4 v53, v[16:19], s[18:19] sc1

	.amdhsa_kernel _Z12wconv_kernel5WDesci
		.amdhsa_group_segment_fixed_size 16640
		.amdhsa_private_segment_fixed_size 0
		.amdhsa_kernarg_size 340
		.amdhsa_user_sgpr_count 2
		.amdhsa_user_sgpr_dispatch_ptr 0
		.amdhsa_user_sgpr_queue_ptr 0
		.amdhsa_user_sgpr_kernarg_segment_ptr 1
		.amdhsa_user_sgpr_dispatch_id 0
		.amdhsa_user_sgpr_kernarg_preload_length 0
		.amdhsa_user_sgpr_kernarg_preload_offset 0
		.amdhsa_user_sgpr_private_segment_size 0
		.amdhsa_uses_dynamic_stack 0
		.amdhsa_enable_private_segment 0
		.amdhsa_system_sgpr_workgroup_id_x 1
		.amdhsa_system_sgpr_workgroup_id_y 1
		.amdhsa_system_sgpr_workgroup_id_z 0
		.amdhsa_system_sgpr_workgroup_info 0
		.amdhsa_system_vgpr_workitem_id 0
		.amdhsa_next_free_vgpr 54
		.amdhsa_next_free_sgpr 34
		.amdhsa_accum_offset 56
		.amdhsa_reserve_vcc 0
		.amdhsa_float_round_mode_32 0
		.amdhsa_float_round_mode_16_64 0
		.amdhsa_float_denorm_mode_32 3
		.amdhsa_float_denorm_mode_16_64 3
		.amdhsa_dx10_clamp 1
		.amdhsa_ieee_mode 1
		.amdhsa_fp16_overflow 0
		.amdhsa_tg_split 0
		.amdhsa_exception_fp_ieee_invalid_op 0
		.amdhsa_exception_fp_denorm_src 0
		.amdhsa_exception_fp_ieee_div_zero 0
		.amdhsa_exception_fp_ieee_overflow 0
		.amdhsa_exception_fp_ieee_underflow 0
		.amdhsa_exception_fp_ieee_inexact 0
		.amdhsa_exception_int_div_zero 0
	.end_amdhsa_kernel

amdhsa.kernels:
  - .agpr_count:     0
    .args:
      - .offset:         0
        .size:           336
        .value_kind:     by_value
      - .offset:         336
        .size:           4
        .value_kind:     by_value
    .group_segment_fixed_size: 16640
    .kernarg_segment_align: 8
    .kernarg_segment_size: 340
    .language:       OpenCL C
    .language_version:
      - 2
      - 0
    .max_flat_workgroup_size: 256
    .name:           _Z12wconv_kernel5WDesci
    .private_segment_fixed_size: 0
    .sgpr_count:     40
    .sgpr_spill_count: 0
    .symbol:         _Z12wconv_kernel5WDesci.kd
    .uniform_work_group_size: 1
    .uses_dynamic_stack: false
    .vgpr_count:     54
    .vgpr_spill_count: 0
    .wavefront_size: 64
  - .agpr_count:     128
    .args:
      - .actual_access:  read_only
        .address_space:  global
        .offset:         0
        .size:           8
        .value_kind:     global_buffer
      - .address_space:  global
        .offset:         8
        .size:           8
        .value_kind:     global_buffer
      - .address_space:  global
        .offset:         16
        .size:           8
        .value_kind:     global_buffer
      - .actual_access:  read_only
        .address_space:  global
        .offset:         24
        .size:           8
        .value_kind:     global_buffer
      - .actual_access:  read_only
        .address_space:  global
        .offset:         32
        .size:           8
        .value_kind:     global_buffer
      - .actual_access:  read_only
        .address_space:  global
        .offset:         40
        .size:           8
        .value_kind:     global_buffer
      - .actual_access:  write_only
        .address_space:  global
        .offset:         48
        .size:           8
        .value_kind:     global_buffer
    .group_segment_fixed_size: 0
    .kernarg_segment_align: 8
    .kernarg_segment_size: 56
    .language:       OpenCL C
    .language_version:
      - 2
      - 0
    .max_flat_workgroup_size: 256
    .name:           _Z8ret_fastPKtS0_S0_S0_PKfS2_Pt
    .private_segment_fixed_size: 0
    .sgpr_count:     85
    .sgpr_spill_count: 0
    .symbol:         _Z8ret_fastPKtS0_S0_S0_PKfS2_Pt.kd
    .uniform_work_group_size: 1
    .uses_dynamic_stack: false
    .vgpr_count:     348
    .vgpr_spill_count: 0
    .wavefront_size: 64
  - .agpr_count:     0
    .args:
      - .actual_access:  read_only
        .address_space:  global
        .offset:         0
        .size:           8
        .value_kind:     global_buffer
      - .actual_access:  read_only
        .address_space:  global
        .offset:         8
        .size:           8
        .value_kind:     global_buffer
      - .actual_access:  read_only
        .address_space:  global
        .offset:         16
        .size:           8
        .value_kind:     global_buffer
      - .actual_access:  read_only
        .address_space:  global
        .offset:         24
        .size:           8
        .value_kind:     global_buffer
      - .actual_access:  write_only
        .address_space:  global
        .offset:         32
        .size:           8
        .value_kind:     global_buffer
      - .actual_access:  write_only
        .address_space:  global
        .offset:         40
        .size:           8
        .value_kind:     global_buffer
      - .actual_access:  read_only
        .address_space:  global
        .offset:         48
        .size:           8
        .value_kind:     global_buffer
      - .actual_access:  read_only
        .address_space:  global
        .offset:         56
        .size:           8
        .value_kind:     global_buffer
    .group_segment_fixed_size: 16
    .kernarg_segment_align: 8
    .kernarg_segment_size: 64
    .language:       OpenCL C
    .language_version:
      - 2
      - 0
    .max_flat_workgroup_size: 256
    .name:           _Z9ln_kernelILb0ELb0EEvPKvPKtS3_PKfPvPtS5_S5_
    .private_segment_fixed_size: 0
    .sgpr_count:     34
    .sgpr_spill_count: 0
    .symbol:         _Z9ln_kernelILb0ELb0EEvPKvPKtS3_PKfPvPtS5_S5_.kd
    .uniform_work_group_size: 1
    .uses_dynamic_stack: false
    .vgpr_count:     62
    .vgpr_spill_count: 0
    .wavefront_size: 64
  - .agpr_count:     0
    .args:
      - .actual_access:  read_only
        .address_space:  global
        .offset:         0
        .size:           8
        .value_kind:     global_buffer
      - .actual_access:  read_only
        .address_space:  global
        .offset:         8
        .size:           8
        .value_kind:     global_buffer
      - .actual_access:  read_only
        .address_space:  global
        .offset:         16
        .size:           8
        .value_kind:     global_buffer
      - .actual_access:  read_only
        .address_space:  global
        .offset:         24
        .size:           8
        .value_kind:     global_buffer
      - .actual_access:  write_only
        .address_space:  global
        .offset:         32
        .size:           8
        .value_kind:     global_buffer
      - .actual_access:  write_only
        .address_space:  global
        .offset:         40
        .size:           8
        .value_kind:     global_buffer
      - .actual_access:  read_only
        .address_space:  global
        .offset:         48
        .size:           8
        .value_kind:     global_buffer
      - .actual_access:  read_only
        .address_space:  global
        .offset:         56
        .size:           8
        .value_kind:     global_buffer
    .group_segment_fixed_size: 16
    .kernarg_segment_align: 8
    .kernarg_segment_size: 64
    .language:       OpenCL C
    .language_version:
      - 2
      - 0
    .max_flat_workgroup_size: 256
    .name:           _Z9ln_kernelILb1ELb1EEvPKvPKtS3_PKfPvPtS5_S5_
    .private_segment_fixed_size: 0
    .sgpr_count:     34
    .sgpr_spill_count: 0
    .symbol:         _Z9ln_kernelILb1ELb1EEvPKvPKtS3_PKfPvPtS5_S5_.kd
    .uniform_work_group_size: 1
    .uses_dynamic_stack: false
    .vgpr_count:     62
    .vgpr_spill_count: 0
    .wavefront_size: 64
  - .agpr_count:     0
    .args:
      - .address_space:  global
        .offset:         0
        .size:           8
        .value_kind:     global_buffer
      - .address_space:  global
        .offset:         8
        .size:           8
        .value_kind:     global_buffer
      - .offset:         16
        .size:           4
        .value_kind:     by_value
      - .offset:         20
        .size:           4
        .value_kind:     by_value
      - .offset:         24
        .size:           4
        .value_kind:     by_value
      - .offset:         28
        .size:           4
        .value_kind:     by_value
      - .offset:         32
        .size:           40
        .value_kind:     by_value
      - .offset:         72
        .size:           4
        .value_kind:     hidden_block_count_x
      - .offset:         76
        .size:           4
        .value_kind:     hidden_block_count_y
      - .offset:         80
        .size:           4
        .value_kind:     hidden_block_count_z
      - .offset:         84
        .size:           2
        .value_kind:     hidden_group_size_x
      - .offset:         86
        .size:           2
        .value_kind:     hidden_group_size_y
      - .offset:         88
        .size:           2
        .value_kind:     hidden_group_size_z
      - .offset:         90
        .size:           2
        .value_kind:     hidden_remainder_x
      - .offset:         92
        .size:           2
        .value_kind:     hidden_remainder_y
      - .offset:         94
        .size:           2
        .value_kind:     hidden_remainder_z
      - .offset:         112
        .size:           8
        .value_kind:     hidden_global_offset_x
      - .offset:         120
        .size:           8
        .value_kind:     hidden_global_offset_y
      - .offset:         128
        .size:           8
        .value_kind:     hidden_global_offset_z
      - .offset:         136
        .size:           2
        .value_kind:     hidden_grid_dims
      - .offset:         192
        .size:           4
        .value_kind:     hidden_dynamic_lds_size
    .group_segment_fixed_size: 0
    .kernarg_segment_align: 8
    .kernarg_segment_size: 328
    .language:       OpenCL C
    .language_version:
      - 2
      - 0
    .max_flat_workgroup_size: 512
    .name:           _Z9gemm_fastILi0ELi2EEvPKtS1_iiii7EpiArgs
    .private_segment_fixed_size: 0
    .sgpr_count:     55
    .sgpr_spill_count: 0
    .symbol:         _Z9gemm_fastILi0ELi2EEvPKtS1_iiii7EpiArgs.kd
    .uniform_work_group_size: 1
    .uses_dynamic_stack: false
    .vgpr_count:     255
    .vgpr_spill_count: 0
    .wavefront_size: 64
  - .agpr_count:     0
    .args:
      - .address_space:  global
        .offset:         0
        .size:           8
        .value_kind:     global_buffer
      - .address_space:  global
        .offset:         8
        .size:           8
        .value_kind:     global_buffer
      - .offset:         16
        .size:           4
        .value_kind:     by_value
      - .offset:         20
        .size:           4
        .value_kind:     by_value
      - .offset:         24
        .size:           4
        .value_kind:     by_value
      - .offset:         28
        .size:           4
        .value_kind:     by_value
      - .offset:         32
        .size:           40
        .value_kind:     by_value
    .group_segment_fixed_size: 0
    .kernarg_segment_align: 8
    .kernarg_segment_size: 72
    .language:       OpenCL C
    .language_version:
      - 2
      - 0
    .max_flat_workgroup_size: 512
    .name:           _Z9gemm_fastILi1ELi1EEvPKtS1_iiii7EpiArgs
    .private_segment_fixed_size: 0
    .sgpr_count:     32
    .sgpr_spill_count: 0
    .symbol:         _Z9gemm_fastILi1ELi1EEvPKtS1_iiii7EpiArgs.kd
    .uniform_work_group_size: 1
    .uses_dynamic_stack: false
    .vgpr_count:     247
    .vgpr_spill_count: 0
    .wavefront_size: 64
  - .agpr_count:     0
    .args:
      - .actual_access:  read_only
        .address_space:  global
        .offset:         0
        .size:           8
        .value_kind:     global_buffer
      - .actual_access:  read_only
        .address_space:  global
        .offset:         8
        .size:           8
        .value_kind:     global_buffer
      - .actual_access:  read_only
        .address_space:  global
        .offset:         16
        .size:           8
        .value_kind:     global_buffer
      - .actual_access:  read_only
        .address_space:  global
        .offset:         24
        .size:           8
        .value_kind:     global_buffer
      - .actual_access:  write_only
        .address_space:  global
        .offset:         32
        .size:           8
        .value_kind:     global_buffer
      - .actual_access:  write_only
        .address_space:  global
        .offset:         40
        .size:           8
        .value_kind:     global_buffer
      - .actual_access:  read_only
        .address_space:  global
        .offset:         48
        .size:           8
        .value_kind:     global_buffer
      - .actual_access:  read_only
        .address_space:  global
        .offset:         56
        .size:           8
        .value_kind:     global_buffer
    .group_segment_fixed_size: 16
    .kernarg_segment_align: 8
    .kernarg_segment_size: 64
    .language:       OpenCL C
    .language_version:
      - 2
      - 0
    .max_flat_workgroup_size: 256
    .name:           _Z9ln_kernelILb0ELb1EEvPKvPKtS3_PKfPvPtS5_S5_
    .private_segment_fixed_size: 0
    .sgpr_count:     34
    .sgpr_spill_count: 0
    .symbol:         _Z9ln_kernelILb0ELb1EEvPKvPKtS3_PKfPvPtS5_S5_.kd
    .uniform_work_group_size: 1
    .uses_dynamic_stack: false
    .vgpr_count:     62
    .vgpr_spill_count: 0
    .wavefront_size: 64
  - .agpr_count:     0
    .args:
      - .address_space:  global
        .offset:         0
        .size:           8
        .value_kind:     global_buffer
      - .address_space:  global
        .offset:         8
        .size:           8
        .value_kind:     global_buffer
      - .offset:         16
        .size:           4
        .value_kind:     by_value
      - .offset:         20
        .size:           4
        .value_kind:     by_value
      - .offset:         24
        .size:           4
        .value_kind:     by_value
      - .offset:         28
        .size:           4
        .value_kind:     by_value
      - .offset:         32
        .size:           40
        .value_kind:     by_value
      - .offset:         72
        .size:           4
        .value_kind:     hidden_block_count_x
      - .offset:         76
        .size:           4
        .value_kind:     hidden_block_count_y
      - .offset:         80
        .size:           4
        .value_kind:     hidden_block_count_z
      - .offset:         84
        .size:           2
        .value_kind:     hidden_group_size_x
      - .offset:         86
        .size:           2
        .value_kind:     hidden_group_size_y
      - .offset:         88
        .size:           2
        .value_kind:     hidden_group_size_z
      - .offset:         90
        .size:           2
        .value_kind:     hidden_remainder_x
      - .offset:         92
        .size:           2
        .value_kind:     hidden_remainder_y
      - .offset:         94
        .size:           2
        .value_kind:     hidden_remainder_z
      - .offset:         112
        .size:           8
        .value_kind:     hidden_global_offset_x
      - .offset:         120
        .size:           8
        .value_kind:     hidden_global_offset_y
      - .offset:         128
        .size:           8
        .value_kind:     hidden_global_offset_z
      - .offset:         136
        .size:           2
        .value_kind:     hidden_grid_dims
      - .offset:         192
        .size:           4
        .value_kind:     hidden_dynamic_lds_size
    .group_segment_fixed_size: 0
    .kernarg_segment_align: 8
    .kernarg_segment_size: 328
    .language:       OpenCL C
    .language_version:
      - 2
      - 0
    .max_flat_workgroup_size: 512
    .name:           _Z9gemm_fastILi2ELi2EEvPKtS1_iiii7EpiArgs
    .private_segment_fixed_size: 0
    .sgpr_count:     53
    .sgpr_spill_count: 0
    .symbol:         _Z9gemm_fastILi2ELi2EEvPKtS1_iiii7EpiArgs.kd
    .uniform_work_group_size: 1
    .uses_dynamic_stack: false
    .vgpr_count:     248
    .vgpr_spill_count: 0
    .wavefront_size: 64
  - .agpr_count:     0
    .args:
      - .actual_access:  read_only
        .address_space:  global
        .offset:         0
        .size:           8
        .value_kind:     global_buffer
      - .actual_access:  read_only
        .address_space:  global
        .offset:         8
        .size:           8
        .value_kind:     global_buffer
      - .actual_access:  read_only
        .address_space:  global
        .offset:         16
        .size:           8
        .value_kind:     global_buffer
      - .actual_access:  read_only
        .address_space:  global
        .offset:         24
        .size:           8
        .value_kind:     global_buffer
      - .actual_access:  write_only
        .address_space:  global
        .offset:         32
        .size:           8
        .value_kind:     global_buffer
      - .actual_access:  write_only
        .address_space:  global
        .offset:         40
        .size:           8
        .value_kind:     global_buffer
      - .actual_access:  read_only
        .address_space:  global
        .offset:         48
        .size:           8
        .value_kind:     global_buffer
      - .actual_access:  read_only
        .address_space:  global
        .offset:         56
        .size:           8
        .value_kind:     global_buffer
    .group_segment_fixed_size: 16
    .kernarg_segment_align: 8
    .kernarg_segment_size: 64
    .language:       OpenCL C
    .language_version:
      - 2
      - 0
    .max_flat_workgroup_size: 256
    .name:           _Z9ln_kernelILb1ELb0EEvPKvPKtS3_PKfPvPtS5_S5_
    .private_segment_fixed_size: 0
    .sgpr_count:     34
    .sgpr_spill_count: 0
    .symbol:         _Z9ln_kernelILb1ELb0EEvPKvPKtS3_PKfPvPtS5_S5_.kd
    .uniform_work_group_size: 1
    .uses_dynamic_stack: false
    .vgpr_count:     62
    .vgpr_spill_count: 0
    .wavefront_size: 64
